# attention QK/PV LDS reads software-pipelined with counted lgkmcnt on top of best5
# speedup vs baseline: 1.0113x; 1.0056x over previous
.LBB0_1173:
	s_mul_hi_u32 s7, s80, 0xaaaaaaab
	s_lshr_b32 s7, s7, 1
	s_mul_i32 s7, s7, 0xfffee000
	s_add_i32 s7, s7, 0
	v_add_u32_e32 v166, s6, v159
	v_add_u32_e32 v167, s6, v161
	v_add_u32_e32 v185, s6, v162
	v_add_u32_e32 v230, s6, v163
	ds_read_b128 v[66:69], v166 offset:32768
	ds_read_b128 v[82:85], v167 offset:32768
	ds_read_b128 v[86:89], v185 offset:32768
	ds_read_b128 v[90:93], v230 offset:32768
	ds_read_b128 v[94:97], v166 offset:32896
	ds_read_b128 v[186:189], v167 offset:32896
	ds_read_b128 v[190:193], v185 offset:32896
	ds_read_b128 v[194:197], v230 offset:32896
	ds_read_b128 v[198:201], v158
	ds_read_b128 v[202:205], v166 offset:33024
	ds_read_b128 v[206:209], v158 offset:1024
	ds_read_b128 v[210:213], v167 offset:33024
	ds_read_b128 v[214:217], v158 offset:2048
	ds_read_b128 v[218:221], v185 offset:33024
	ds_read_b128 v[222:225], v158 offset:3072
	s_waitcnt lgkmcnt(14)
	v_mfma_f32_32x32x16_bf16 v[66:81], v[66:69], v[126:129], 0
	ds_read_b128 v[226:229], v230 offset:33024
	s_waitcnt lgkmcnt(14)
	v_mfma_f32_32x32x16_bf16 v[66:81], v[82:85], v[122:125], v[66:81]
	s_waitcnt lgkmcnt(13)
	v_mfma_f32_32x32x16_bf16 v[66:81], v[86:89], v[118:121], v[66:81]
	s_waitcnt lgkmcnt(12)
	v_mfma_f32_32x32x16_bf16 v[66:81], v[90:93], v[114:117], v[66:81]
	s_waitcnt lgkmcnt(11)
	v_mfma_f32_32x32x16_bf16 v[66:81], v[94:97], v[110:113], v[66:81]
	s_waitcnt lgkmcnt(10)
	v_mfma_f32_32x32x16_bf16 v[66:81], v[186:189], v[106:109], v[66:81]
	ds_read_b128 v[186:189], v166 offset:45056
	s_waitcnt lgkmcnt(10)
	v_mfma_f32_32x32x16_bf16 v[66:81], v[190:193], v[102:105], v[66:81]
	ds_read_b128 v[190:193], v167 offset:45056
	s_waitcnt lgkmcnt(10)
	v_mfma_f32_32x32x16_bf16 v[66:81], v[194:197], v[98:101], v[66:81]
	ds_read_b128 v[194:197], v185 offset:45056
	s_waitcnt lgkmcnt(9)
	v_mfma_f32_32x32x16_bf16 v[66:81], v[202:205], v[198:201], v[66:81]
	ds_read_b128 v[202:205], v230 offset:45056
	s_waitcnt lgkmcnt(8)
	v_mfma_f32_32x32x16_bf16 v[66:81], v[210:213], v[206:209], v[66:81]
	ds_read_b128 v[210:213], v166 offset:45184
	s_waitcnt lgkmcnt(7)
	v_mfma_f32_32x32x16_bf16 v[66:81], v[218:221], v[214:217], v[66:81]
	ds_read_b128 v[218:221], v167 offset:45184
	s_waitcnt lgkmcnt(6)
	v_mfma_f32_32x32x16_bf16 v[66:81], v[226:229], v[222:225], v[66:81]
	ds_read_b128 v[226:229], v185 offset:45184
	s_waitcnt lgkmcnt(6)
	v_mfma_f32_32x32x16_bf16 v[82:97], v[186:189], v[126:129], 0
	ds_read_b128 v[186:189], v230 offset:45184
	s_add_i32 s6, s78, 1
	s_min_u32 s6, s6, s14
	s_waitcnt lgkmcnt(6)
	v_mfma_f32_32x32x16_bf16 v[82:97], v[190:193], v[122:125], v[82:97]
	ds_read_b128 v[246:249], v166 offset:45312
	s_lshl_b32 s10, s6, 6
	s_waitcnt lgkmcnt(6)
	v_mfma_f32_32x32x16_bf16 v[82:97], v[194:197], v[118:121], v[82:97]
	ds_read_b128 v[242:245], v167 offset:45312
	s_cmp_lt_u32 s6, 4
	s_cselect_b32 s6, s74, s15
	s_add_i32 s6, s6, s10
	s_waitcnt lgkmcnt(6)
	v_mfma_f32_32x32x16_bf16 v[82:97], v[202:205], v[114:117], v[82:97]
	ds_read_b128 v[238:241], v185 offset:45312
	s_mul_hi_i32 s11, s6, 0x1080
	s_mulk_i32 s6, 0x1080
	s_waitcnt lgkmcnt(6)
	v_mfma_f32_32x32x16_bf16 v[82:97], v[210:213], v[110:113], v[82:97]
	ds_read_b128 v[234:237], v230 offset:45312
	s_add_u32 s10, s3, s6
	s_addc_u32 s11, s35, s11
	s_add_i32 s6, s7, s30
	s_waitcnt lgkmcnt(6)
	v_mfma_f32_32x32x16_bf16 v[82:97], v[218:221], v[106:109], v[82:97]
	s_add_i32 s6, s6, s8
	s_add_i32 m0, s6, 0x1a000
	s_nop 0
	global_load_lds_dwordx4 v232, s[10:11]
	s_waitcnt lgkmcnt(5)
	v_mfma_f32_32x32x16_bf16 v[82:97], v[226:229], v[102:105], v[82:97]
	s_add_i32 m0, s6, 0x1a400
	s_waitcnt lgkmcnt(4)
	v_mfma_f32_32x32x16_bf16 v[82:97], v[186:189], v[98:101], v[82:97]
	global_load_lds_dwordx4 v251, s[10:11]
	s_add_i32 m0, s6, 0x1a800
	s_waitcnt lgkmcnt(3)
	v_mfma_f32_32x32x16_bf16 v[82:97], v[246:249], v[198:201], v[82:97]
	s_waitcnt lgkmcnt(2)
	v_mfma_f32_32x32x16_bf16 v[82:97], v[242:245], v[206:209], v[82:97]
	global_load_lds_dwordx4 v252, s[10:11]
	s_waitcnt lgkmcnt(1)
	v_mfma_f32_32x32x16_bf16 v[82:97], v[238:241], v[214:217], v[82:97]
	s_waitcnt lgkmcnt(0)
	v_mfma_f32_32x32x16_bf16 v[82:97], v[234:237], v[222:225], v[82:97]
	v_exp_f32_e32 v194, v130
	v_add_f32_e32 v130, 0, v178
	v_add_f32_e32 v130, v182, v130
	v_add_f32_e32 v130, v179, v130
	v_add_f32_e32 v130, v183, v130
	v_add_f32_e32 v130, v180, v130
	v_add_f32_e32 v130, v184, v130
	v_add_f32_e32 v130, v177, v130
	v_add_f32_e32 v130, v181, v130
	v_add_f32_e32 v130, v171, v130
	v_add_f32_e32 v130, v175, v130
	v_add_f32_e32 v130, v172, v130
	v_add_f32_e32 v130, v176, v130
	v_exp_f32_e32 v146, v146
	v_add_f32_e32 v130, v168, v130
	v_exp_f32_e32 v147, v147
	v_add_f32_e32 v130, v173, v130
	v_exp_f32_e32 v167, v144
	v_add_f32_e32 v130, v169, v130
	v_exp_f32_e32 v185, v145
	v_add_f32_e32 v130, v174, v130
	v_exp_f32_e32 v186, v142
	v_add_f32_e32 v130, v146, v130
	v_exp_f32_e32 v187, v143
	v_add_f32_e32 v130, v147, v130
	v_exp_f32_e32 v188, v140
	v_add_f32_e32 v130, v167, v130
	v_exp_f32_e32 v189, v141
	v_add_f32_e32 v130, v185, v130
	v_exp_f32_e32 v190, v138
	v_add_f32_e32 v130, v186, v130
	v_exp_f32_e32 v191, v139
	v_add_f32_e32 v130, v187, v130
	v_exp_f32_e32 v192, v136
	v_add_f32_e32 v130, v188, v130
	v_exp_f32_e32 v193, v137
	v_add_f32_e32 v130, v189, v130
	v_exp_f32_e32 v132, v132
	v_add_f32_e32 v130, v190, v130
	v_exp_f32_e32 v133, v133
	v_add_f32_e32 v130, v191, v130
	v_add_f32_e32 v130, v192, v130
	v_exp_f32_e32 v195, v131
	v_add_f32_e32 v130, v193, v130
	v_add_f32_e32 v130, v132, v130
	v_add_f32_e32 v130, v133, v130
	v_add_f32_e32 v130, v194, v130
	v_add_f32_e32 v136, v195, v130
	v_mov_b32_e32 v137, v136
	v_cvt_pk_bf16_f32 v138, v178, v182
	v_cvt_pk_bf16_f32 v139, v179, v183
	v_cvt_pk_bf16_f32 v140, v180, v184
	v_cvt_pk_bf16_f32 v141, v177, v181
	v_cvt_pk_bf16_f32 v142, v171, v175
	v_cvt_pk_bf16_f32 v143, v172, v176
	v_cvt_pk_bf16_f32 v144, v168, v173
	v_cvt_pk_bf16_f32 v145, v169, v174
	v_cvt_pk_bf16_f32 v166, v146, v147
	v_cvt_pk_bf16_f32 v167, v167, v185
	v_cvt_pk_bf16_f32 v168, v186, v187
	v_cvt_pk_bf16_f32 v169, v188, v189
	s_nop 1
	v_permlane32_swap_b32_e32 v136, v137
	v_permlane32_swap_b32_e32 v138, v140
	v_permlane32_swap_b32_e32 v167, v169
	v_cvt_pk_bf16_f32 v130, v190, v191
	v_cvt_pk_bf16_f32 v131, v192, v193
	v_cvt_pk_bf16_f32 v132, v132, v133
	v_cvt_pk_bf16_f32 v133, v194, v195
	v_permlane32_swap_b32_e32 v139, v141
	v_permlane32_swap_b32_e32 v142, v144
	v_permlane32_swap_b32_e32 v143, v145
	v_permlane32_swap_b32_e32 v166, v168
	v_permlane32_swap_b32_e32 v130, v132
	v_permlane32_swap_b32_e32 v131, v133
	ds_read_b64_tr_b16 v[172:173], v160 offset:0
	ds_read_b64_tr_b16 v[174:175], v160 offset:0x800
	ds_read_b64_tr_b16 v[176:177], v160 offset:0x1000
	ds_read_b64_tr_b16 v[178:179], v160 offset:0x1800
	ds_read_b64_tr_b16 v[180:181], v160 offset:0x2000
	ds_read_b64_tr_b16 v[182:183], v160 offset:0x2800
	ds_read_b64_tr_b16 v[184:185], v160 offset:0x3000
	ds_read_b64_tr_b16 v[186:187], v160 offset:0x3800
	s_nop 0
	s_waitcnt lgkmcnt(6)
	v_mfma_f32_32x32x16_bf16 v[2:17], v[138:141], v[172:175], v[2:17]
	ds_read_b64_tr_b16 v[172:173], v160 offset:0x200
	ds_read_b64_tr_b16 v[174:175], v160 offset:0xa00
	s_waitcnt lgkmcnt(6)
	v_mfma_f32_32x32x16_bf16 v[2:17], v[142:145], v[176:179], v[2:17]
	ds_read_b64_tr_b16 v[176:177], v160 offset:0x1200
	ds_read_b64_tr_b16 v[178:179], v160 offset:0x1a00
	s_waitcnt lgkmcnt(6)
	v_mfma_f32_32x32x16_bf16 v[2:17], v[166:169], v[180:183], v[2:17]
	ds_read_b64_tr_b16 v[180:181], v160 offset:0x2200
	ds_read_b64_tr_b16 v[182:183], v160 offset:0x2a00
	ds_read_b64_tr_b16 v[188:189], v160 offset:0x3200
	ds_read_b64_tr_b16 v[190:191], v160 offset:0x3a00
	s_waitcnt lgkmcnt(8)
	v_mfma_f32_32x32x16_bf16 v[2:17], v[130:133], v[184:187], v[2:17]
	s_waitcnt lgkmcnt(6)
	v_mfma_f32_32x32x16_bf16 v[50:65], v[138:141], v[172:175], v[50:65]
	ds_read_b64_tr_b16 v[172:173], v160 offset:0x400
	ds_read_b64_tr_b16 v[174:175], v160 offset:0xc00
	s_waitcnt lgkmcnt(6)
	v_mfma_f32_32x32x16_bf16 v[50:65], v[142:145], v[176:179], v[50:65]
	ds_read_b64_tr_b16 v[176:177], v160 offset:0x1400
	ds_read_b64_tr_b16 v[178:179], v160 offset:0x1c00
	s_waitcnt lgkmcnt(6)
	v_mfma_f32_32x32x16_bf16 v[50:65], v[166:169], v[180:183], v[50:65]
	ds_read_b64_tr_b16 v[180:181], v160 offset:0x2400
	ds_read_b64_tr_b16 v[182:183], v160 offset:0x2c00
	ds_read_b64_tr_b16 v[184:185], v160 offset:0x3400
	ds_read_b64_tr_b16 v[186:187], v160 offset:0x3c00
	s_waitcnt lgkmcnt(8)
	v_mfma_f32_32x32x16_bf16 v[50:65], v[130:133], v[188:191], v[50:65]
	s_waitcnt lgkmcnt(6)
	v_mfma_f32_32x32x16_bf16 v[34:49], v[138:141], v[172:175], v[34:49]
	ds_read_b64_tr_b16 v[172:173], v160 offset:0x600
	ds_read_b64_tr_b16 v[174:175], v160 offset:0xe00
	s_waitcnt lgkmcnt(6)
	v_mfma_f32_32x32x16_bf16 v[34:49], v[142:145], v[176:179], v[34:49]
	ds_read_b64_tr_b16 v[176:177], v160 offset:0x1600
	ds_read_b64_tr_b16 v[178:179], v160 offset:0x1e00
	s_waitcnt lgkmcnt(6)
	v_mfma_f32_32x32x16_bf16 v[34:49], v[166:169], v[180:183], v[34:49]
	ds_read_b64_tr_b16 v[180:181], v160 offset:0x2600
	ds_read_b64_tr_b16 v[182:183], v160 offset:0x2e00
	ds_read_b64_tr_b16 v[188:189], v160 offset:0x3600
	ds_read_b64_tr_b16 v[190:191], v160 offset:0x3e00
	s_waitcnt lgkmcnt(8)
	v_mfma_f32_32x32x16_bf16 v[34:49], v[130:133], v[184:187], v[34:49]
	v_max_f32_e32 v146, v67, v67
	v_max_f32_e32 v147, v66, v66
	v_max_f32_e32 v146, v147, v146
	v_max3_f32 v146, v146, v68, v69
	v_max3_f32 v146, v146, v70, v71
	s_waitcnt lgkmcnt(6)
	v_mfma_f32_32x32x16_bf16 v[18:33], v[138:141], v[172:175], v[18:33]
	v_max3_f32 v138, v146, v72, v73
	v_max3_f32 v138, v138, v74, v75
	v_max3_f32 v138, v138, v76, v77
	v_max3_f32 v138, v138, v78, v79
	v_max3_f32 v138, v138, v80, v81
	v_max3_f32 v138, v138, v82, v83
	v_max3_f32 v138, v138, v84, v85
	v_max3_f32 v138, v138, v86, v87
	v_max3_f32 v138, v138, v88, v89
	v_max3_f32 v138, v138, v90, v91
	v_max3_f32 v138, v138, v92, v93
	v_max3_f32 v138, v138, v94, v95
	v_max3_f32 v138, v138, v96, v97
	v_mov_b32_e32 v139, v138
	s_nop 1
	v_permlane32_swap_b32_e32 v138, v139
	v_max_f32_e32 v139, v139, v139
	v_max_f32_e32 v138, v138, v138
	v_max_f32_e32 v138, v138, v139
	v_sub_f32_e32 v139, v138, v165
	s_waitcnt lgkmcnt(4)
	v_mfma_f32_32x32x16_bf16 v[18:33], v[142:145], v[176:179], v[18:33]
	v_cmp_ge_f32_e32 vcc, s65, v139
	s_waitcnt vmcnt(3) lgkmcnt(0)
	s_barrier
	s_cmp_eq_u64 vcc, exec
	s_cselect_b64 s[6:7], -1, 0
	s_cmp_lt_u32 s78, 4
	s_cselect_b32 s12, s74, s15
	s_add_i32 s12, s12, s9
	s_mul_hi_i32 s13, s12, 0x1080
	s_mulk_i32 s12, 0x1080
	s_add_u32 s12, s3, s12
	s_mov_b32 m0, s70
	s_addc_u32 s13, s35, s13
	global_load_lds_dwordx4 v253, s[12:13]
	s_mov_b32 m0, s72
	v_mfma_f32_32x32x16_bf16 v[18:33], v[166:169], v[180:183], v[18:33]
	global_load_lds_dwordx4 v254, s[12:13]
	v_max_f32_e32 v139, v165, v165
	v_max_f32_e32 v138, v139, v138
	v_sub_f32_e32 v139, v165, v138
	v_mul_f32_e32 v139, 0x3dd53b94, v139
	v_exp_f32_e32 v139, v139
	v_mfma_f32_32x32x16_bf16 v[18:33], v[130:133], v[188:191], v[18:33]
	v_cndmask_b32_e64 v167, v139, 1.0, s[6:7]
	v_cmp_gt_f32_e32 vcc, 1.0, v167
	s_cbranch_vccz .LBB0_1177
	s_and_saveexec_b64 s[12:13], s[4:5]
	ds_write_b32 v155, v167 offset:128
	s_or_b64 exec, exec, s[12:13]
	s_waitcnt lgkmcnt(0)
	v_add_u32_e32 v139, s69, v134
	ds_read_b128 v[130:133], v139 offset:224
	ds_read_b128 v[140:143], v139 offset:192
	ds_read_b128 v[144:147], v139 offset:160
	ds_read_b128 v[172:175], v139 offset:128
	s_waitcnt lgkmcnt(0)
	v_pk_mul_f32 v[14:15], v[14:15], v[130:131]
	v_pk_mul_f32 v[10:11], v[10:11], v[140:141]
	v_pk_mul_f32 v[6:7], v[6:7], v[144:145]
	v_pk_mul_f32 v[16:17], v[16:17], v[132:133]
	v_pk_mul_f32 v[12:13], v[12:13], v[142:143]
	v_pk_mul_f32 v[8:9], v[8:9], v[146:147]
	v_pk_mul_f32 v[4:5], v[4:5], v[174:175]
	v_pk_mul_f32 v[2:3], v[2:3], v[172:173]
	v_pk_mul_f32 v[62:63], v[62:63], v[130:131]
	v_pk_mul_f32 v[58:59], v[58:59], v[140:141]
	v_pk_mul_f32 v[54:55], v[54:55], v[144:145]
	v_pk_mul_f32 v[64:65], v[64:65], v[132:133]
	v_pk_mul_f32 v[60:61], v[60:61], v[142:143]
	v_pk_mul_f32 v[56:57], v[56:57], v[146:147]
	v_pk_mul_f32 v[52:53], v[52:53], v[174:175]
	v_pk_mul_f32 v[50:51], v[50:51], v[172:173]
	v_pk_mul_f32 v[46:47], v[46:47], v[130:131]
	v_pk_mul_f32 v[42:43], v[42:43], v[140:141]
	v_pk_mul_f32 v[38:39], v[38:39], v[144:145]
	v_pk_mul_f32 v[48:49], v[48:49], v[132:133]
	v_pk_mul_f32 v[44:45], v[44:45], v[142:143]
	v_pk_mul_f32 v[40:41], v[40:41], v[146:147]
	v_pk_mul_f32 v[36:37], v[36:37], v[174:175]
	v_pk_mul_f32 v[34:35], v[34:35], v[172:173]
	v_pk_mul_f32 v[30:31], v[30:31], v[130:131]
	v_pk_mul_f32 v[26:27], v[26:27], v[140:141]
	v_pk_mul_f32 v[22:23], v[22:23], v[144:145]
	v_pk_mul_f32 v[32:33], v[32:33], v[132:133]
	v_pk_mul_f32 v[28:29], v[28:29], v[142:143]
	v_pk_mul_f32 v[24:25], v[24:25], v[146:147]
	v_pk_mul_f32 v[20:21], v[20:21], v[174:175]
	v_pk_mul_f32 v[18:19], v[18:19], v[172:173]
.LBB0_1177:
	v_cndmask_b32_e64 v130, v138, v165, s[6:7]
	s_mul_hi_u32 s12, s79, 0xaaaaaaab
	v_mul_f32_e32 v131, 0xbdd53b94, v130
	s_lshr_b32 s12, s12, 1
	v_fmamk_f32 v66, v66, 0x3dd53b94, v131
	v_fmamk_f32 v68, v68, 0x3dd53b94, v131
	v_fmamk_f32 v70, v70, 0x3dd53b94, v131
	v_fmamk_f32 v72, v72, 0x3dd53b94, v131
	s_mul_i32 s12, s12, 0xfffee000
	v_fmamk_f32 v74, v74, 0x3dd53b94, v131
	v_fmamk_f32 v76, v76, 0x3dd53b94, v131
	v_fmamk_f32 v78, v78, 0x3dd53b94, v131
	v_fmamk_f32 v80, v80, 0x3dd53b94, v131
	v_fmamk_f32 v132, v82, 0x3dd53b94, v131
	v_fmamk_f32 v133, v84, 0x3dd53b94, v131
	v_fmamk_f32 v146, v86, 0x3dd53b94, v131
	v_fmamk_f32 v147, v88, 0x3dd53b94, v131
	v_fmamk_f32 v165, v90, 0x3dd53b94, v131
	v_fmamk_f32 v166, v92, 0x3dd53b94, v131
	v_fmamk_f32 v168, v94, 0x3dd53b94, v131
	v_fmamk_f32 v169, v96, 0x3dd53b94, v131
	v_exp_f32_e32 v171, v66
	v_exp_f32_e32 v224, v68
	v_exp_f32_e32 v225, v70
	v_exp_f32_e32 v226, v72
	v_fmamk_f32 v66, v67, 0x3dd53b94, v131
	v_fmamk_f32 v67, v69, 0x3dd53b94, v131
	v_fmamk_f32 v68, v71, 0x3dd53b94, v131
	v_fmamk_f32 v69, v73, 0x3dd53b94, v131
	v_fmamk_f32 v70, v75, 0x3dd53b94, v131
	v_fmamk_f32 v71, v77, 0x3dd53b94, v131
	v_fmamk_f32 v72, v79, 0x3dd53b94, v131
	v_fmamk_f32 v73, v81, 0x3dd53b94, v131
	v_fmamk_f32 v231, v83, 0x3dd53b94, v131
	v_fmamk_f32 v233, v85, 0x3dd53b94, v131
	v_fmamk_f32 v234, v87, 0x3dd53b94, v131
	v_fmamk_f32 v235, v89, 0x3dd53b94, v131
	v_fmamk_f32 v236, v91, 0x3dd53b94, v131
	v_fmamk_f32 v245, v93, 0x3dd53b94, v131
	v_fmamk_f32 v246, v95, 0x3dd53b94, v131
	v_fmac_f32_e32 v131, 0x3dd53b94, v97
	s_add_i32 s12, s12, 0
	v_exp_f32_e32 v227, v74
	v_exp_f32_e32 v228, v76
	v_exp_f32_e32 v229, v78
	v_exp_f32_e32 v230, v80
	v_exp_f32_e32 v237, v66
	v_exp_f32_e32 v238, v67
	v_exp_f32_e32 v239, v68
	v_exp_f32_e32 v240, v69
	v_exp_f32_e32 v241, v70
	v_exp_f32_e32 v242, v71
	v_exp_f32_e32 v243, v72
	v_exp_f32_e32 v244, v73
	v_add_u32_e32 v196, s16, v159
	v_add_u32_e32 v204, s16, v161
	v_add_u32_e32 v212, s16, v162
	v_add_u32_e32 v220, s16, v163
	ds_read_b128 v[66:69], v196 offset:32768
	ds_read_b128 v[82:85], v204 offset:32768
	ds_read_b128 v[86:89], v212 offset:32768
	ds_read_b128 v[90:93], v220 offset:32768
	ds_read_b128 v[94:97], v196 offset:32896
	ds_read_b128 v[138:141], v204 offset:32896
	ds_read_b128 v[142:145], v212 offset:32896
	ds_read_b128 v[172:175], v220 offset:32896
	ds_read_b128 v[176:179], v158
	ds_read_b128 v[180:183], v196 offset:33024
	ds_read_b128 v[184:187], v158 offset:1024
	ds_read_b128 v[188:191], v204 offset:33024
	ds_read_b128 v[192:195], v158 offset:2048
	ds_read_b128 v[200:203], v212 offset:33024
	ds_read_b128 v[208:211], v158 offset:3072
	s_waitcnt lgkmcnt(14)
	v_mfma_f32_32x32x16_bf16 v[66:81], v[66:69], v[126:129], 0
	ds_read_b128 v[216:219], v220 offset:33024
	s_waitcnt lgkmcnt(14)
	v_mfma_f32_32x32x16_bf16 v[66:81], v[82:85], v[122:125], v[66:81]
	s_waitcnt lgkmcnt(13)
	v_mfma_f32_32x32x16_bf16 v[66:81], v[86:89], v[118:121], v[66:81]
	s_waitcnt lgkmcnt(12)
	v_mfma_f32_32x32x16_bf16 v[66:81], v[90:93], v[114:117], v[66:81]
	s_waitcnt lgkmcnt(11)
	v_mfma_f32_32x32x16_bf16 v[66:81], v[94:97], v[110:113], v[66:81]
	s_waitcnt lgkmcnt(10)
	v_mfma_f32_32x32x16_bf16 v[66:81], v[138:141], v[106:109], v[66:81]
	ds_read_b128 v[138:141], v196 offset:45056
	s_waitcnt lgkmcnt(10)
	v_mfma_f32_32x32x16_bf16 v[66:81], v[142:145], v[102:105], v[66:81]
	ds_read_b128 v[142:145], v204 offset:45056
	s_waitcnt lgkmcnt(10)
	v_mfma_f32_32x32x16_bf16 v[66:81], v[172:175], v[98:101], v[66:81]
	ds_read_b128 v[172:175], v212 offset:45056
	s_waitcnt lgkmcnt(9)
	v_mfma_f32_32x32x16_bf16 v[66:81], v[180:183], v[176:179], v[66:81]
	ds_read_b128 v[180:183], v220 offset:45056
	s_waitcnt lgkmcnt(8)
	v_mfma_f32_32x32x16_bf16 v[66:81], v[188:191], v[184:187], v[66:81]
	ds_read_b128 v[188:191], v196 offset:45184
	s_waitcnt lgkmcnt(7)
	v_mfma_f32_32x32x16_bf16 v[66:81], v[200:203], v[192:195], v[66:81]
	ds_read_b128 v[200:203], v204 offset:45184
	s_waitcnt lgkmcnt(6)
	v_mfma_f32_32x32x16_bf16 v[66:81], v[216:219], v[208:211], v[66:81]
	ds_read_b128 v[216:219], v212 offset:45184
	s_waitcnt lgkmcnt(6)
	v_mfma_f32_32x32x16_bf16 v[82:97], v[138:141], v[126:129], 0
	ds_read_b128 v[138:141], v220 offset:45184
	s_add_i32 s78, s78, 2
	s_min_u32 s6, s78, s14
	s_lshl_b32 s7, s6, 6
	s_cmp_lt_u32 s6, 4
	s_cselect_b32 s6, s74, s15
	s_add_i32 s6, s6, s7
	s_mul_hi_i32 s7, s6, 0x1080
	s_waitcnt lgkmcnt(6)
	v_mfma_f32_32x32x16_bf16 v[82:97], v[142:145], v[122:125], v[82:97]
	ds_read_b128 v[196:199], v196 offset:45312
	s_mulk_i32 s6, 0x1080
	s_waitcnt lgkmcnt(6)
	v_mfma_f32_32x32x16_bf16 v[82:97], v[172:175], v[118:121], v[82:97]
	ds_read_b128 v[204:207], v204 offset:45312
	s_waitcnt lgkmcnt(6)
	v_mfma_f32_32x32x16_bf16 v[82:97], v[180:183], v[114:117], v[82:97]
	ds_read_b128 v[212:215], v212 offset:45312
	s_waitcnt lgkmcnt(6)
	v_mfma_f32_32x32x16_bf16 v[82:97], v[188:191], v[110:113], v[82:97]
	ds_read_b128 v[220:223], v220 offset:45312
	s_add_u32 s6, s3, s6
	s_addc_u32 s7, s35, s7
	s_add_i32 s12, s12, s30
	s_waitcnt lgkmcnt(6)
	v_mfma_f32_32x32x16_bf16 v[82:97], v[200:203], v[106:109], v[82:97]
	s_add_i32 s12, s12, s8
	s_add_i32 m0, s12, 0x20000
	s_nop 0
	global_load_lds_dwordx4 v232, s[6:7]
	s_waitcnt lgkmcnt(5)
	v_mfma_f32_32x32x16_bf16 v[82:97], v[216:219], v[102:105], v[82:97]
	s_add_i32 m0, s12, 0x20400
	s_waitcnt lgkmcnt(4)
	v_mfma_f32_32x32x16_bf16 v[82:97], v[138:141], v[98:101], v[82:97]
	global_load_lds_dwordx4 v251, s[6:7]
	s_add_i32 m0, s12, 0x20800
	s_waitcnt lgkmcnt(3)
	v_mfma_f32_32x32x16_bf16 v[82:97], v[196:199], v[176:179], v[82:97]
	s_waitcnt lgkmcnt(2)
	v_mfma_f32_32x32x16_bf16 v[82:97], v[204:207], v[184:187], v[82:97]
	global_load_lds_dwordx4 v252, s[6:7]
	s_waitcnt lgkmcnt(1)
	v_mfma_f32_32x32x16_bf16 v[82:97], v[212:215], v[192:195], v[82:97]
	s_waitcnt lgkmcnt(0)
	v_mfma_f32_32x32x16_bf16 v[82:97], v[220:223], v[208:211], v[82:97]
	v_add_f32_e32 v138, 0, v171
	v_add_f32_e32 v138, v237, v138
	v_add_f32_e32 v138, v224, v138
	v_add_f32_e32 v138, v238, v138
	v_add_f32_e32 v138, v225, v138
	v_add_f32_e32 v138, v239, v138
	v_add_f32_e32 v138, v226, v138
	v_add_f32_e32 v138, v240, v138
	v_add_f32_e32 v138, v227, v138
	v_add_f32_e32 v138, v241, v138
	v_add_f32_e32 v138, v228, v138
	v_add_f32_e32 v138, v242, v138
	v_exp_f32_e32 v132, v132
	v_add_f32_e32 v138, v229, v138
	v_exp_f32_e32 v172, v231
	v_add_f32_e32 v138, v243, v138
	v_exp_f32_e32 v133, v133
	v_add_f32_e32 v138, v230, v138
	v_exp_f32_e32 v173, v233
	v_add_f32_e32 v138, v244, v138
	v_exp_f32_e32 v146, v146
	v_add_f32_e32 v138, v132, v138
	v_exp_f32_e32 v174, v234
	v_add_f32_e32 v138, v172, v138
	v_exp_f32_e32 v147, v147
	v_add_f32_e32 v138, v133, v138
	v_exp_f32_e32 v175, v235
	v_add_f32_e32 v138, v173, v138
	v_exp_f32_e32 v165, v165
	v_add_f32_e32 v138, v146, v138
	v_exp_f32_e32 v176, v236
	v_add_f32_e32 v138, v174, v138
	v_exp_f32_e32 v166, v166
	v_add_f32_e32 v138, v147, v138
	v_exp_f32_e32 v177, v245
	v_add_f32_e32 v138, v175, v138
	v_exp_f32_e32 v168, v168
	v_add_f32_e32 v138, v165, v138
	v_exp_f32_e32 v178, v246
	v_add_f32_e32 v138, v176, v138
	v_exp_f32_e32 v169, v169
	v_add_f32_e32 v138, v166, v138
	v_exp_f32_e32 v131, v131
	v_add_f32_e32 v138, v177, v138
	v_add_f32_e32 v138, v168, v138
	v_add_f32_e32 v138, v178, v138
	v_add_f32_e32 v138, v169, v138
	v_add_f32_e32 v185, v131, v138
	v_mov_b32_e32 v186, v185
	s_nop 1
	v_permlane32_swap_b32_e32 v185, v186
	v_cvt_pk_bf16_f32 v138, v171, v237
	v_cvt_pk_bf16_f32 v139, v224, v238
	v_cvt_pk_bf16_f32 v140, v225, v239
	v_cvt_pk_bf16_f32 v141, v226, v240
	v_cvt_pk_bf16_f32 v142, v227, v241
	v_cvt_pk_bf16_f32 v143, v228, v242
	v_cvt_pk_bf16_f32 v144, v229, v243
	v_cvt_pk_bf16_f32 v145, v230, v244
	v_cvt_pk_bf16_f32 v172, v132, v172
	v_cvt_pk_bf16_f32 v173, v133, v173
	v_cvt_pk_bf16_f32 v174, v146, v174
	v_cvt_pk_bf16_f32 v175, v147, v175
	v_cvt_pk_bf16_f32 v176, v165, v176
	v_cvt_pk_bf16_f32 v177, v166, v177
	v_cvt_pk_bf16_f32 v178, v168, v178
	v_cvt_pk_bf16_f32 v179, v169, v131
	s_nop 0
	v_permlane32_swap_b32_e32 v138, v140
	v_permlane32_swap_b32_e32 v139, v141
	v_permlane32_swap_b32_e32 v142, v144
	v_permlane32_swap_b32_e32 v143, v145
	v_permlane32_swap_b32_e32 v172, v174
	v_permlane32_swap_b32_e32 v173, v175
	v_permlane32_swap_b32_e32 v176, v178
	v_permlane32_swap_b32_e32 v177, v179
	ds_read_b64_tr_b16 v[180:181], v156 offset:0
	ds_read_b64_tr_b16 v[182:183], v156 offset:0x800
	ds_read_b64_tr_b16 v[188:189], v156 offset:0x1000
	ds_read_b64_tr_b16 v[190:191], v156 offset:0x1800
	ds_read_b64_tr_b16 v[192:193], v156 offset:0x2000
	ds_read_b64_tr_b16 v[194:195], v156 offset:0x2800
	ds_read_b64_tr_b16 v[196:197], v156 offset:0x3000
	ds_read_b64_tr_b16 v[198:199], v156 offset:0x3800
	s_nop 0
	s_waitcnt lgkmcnt(6)
	v_mfma_f32_32x32x16_bf16 v[2:17], v[138:141], v[180:183], v[2:17]
	ds_read_b64_tr_b16 v[180:181], v156 offset:0x200
	ds_read_b64_tr_b16 v[182:183], v156 offset:0xa00
	s_waitcnt lgkmcnt(6)
	v_mfma_f32_32x32x16_bf16 v[2:17], v[142:145], v[188:191], v[2:17]
	ds_read_b64_tr_b16 v[188:189], v156 offset:0x1200
	ds_read_b64_tr_b16 v[190:191], v156 offset:0x1a00
	s_waitcnt lgkmcnt(6)
	v_mfma_f32_32x32x16_bf16 v[2:17], v[172:175], v[192:195], v[2:17]
	ds_read_b64_tr_b16 v[192:193], v156 offset:0x2200
	ds_read_b64_tr_b16 v[194:195], v156 offset:0x2a00
	ds_read_b64_tr_b16 v[200:201], v156 offset:0x3200
	ds_read_b64_tr_b16 v[202:203], v156 offset:0x3a00
	s_waitcnt lgkmcnt(8)
	v_mfma_f32_32x32x16_bf16 v[2:17], v[176:179], v[196:199], v[2:17]
	s_waitcnt lgkmcnt(6)
	v_mfma_f32_32x32x16_bf16 v[50:65], v[138:141], v[180:183], v[50:65]
	ds_read_b64_tr_b16 v[180:181], v156 offset:0x400
	ds_read_b64_tr_b16 v[182:183], v156 offset:0xc00
	s_waitcnt lgkmcnt(6)
	v_mfma_f32_32x32x16_bf16 v[50:65], v[142:145], v[188:191], v[50:65]
	ds_read_b64_tr_b16 v[188:189], v156 offset:0x1400
	ds_read_b64_tr_b16 v[190:191], v156 offset:0x1c00
	s_waitcnt lgkmcnt(6)
	v_mfma_f32_32x32x16_bf16 v[50:65], v[172:175], v[192:195], v[50:65]
	ds_read_b64_tr_b16 v[192:193], v156 offset:0x2400
	ds_read_b64_tr_b16 v[194:195], v156 offset:0x2c00
	ds_read_b64_tr_b16 v[196:197], v156 offset:0x3400
	ds_read_b64_tr_b16 v[198:199], v156 offset:0x3c00
	s_waitcnt lgkmcnt(8)
	v_mfma_f32_32x32x16_bf16 v[50:65], v[176:179], v[200:203], v[50:65]
	s_waitcnt lgkmcnt(6)
	v_mfma_f32_32x32x16_bf16 v[34:49], v[138:141], v[180:183], v[34:49]
	ds_read_b64_tr_b16 v[180:181], v156 offset:0x600
	ds_read_b64_tr_b16 v[182:183], v156 offset:0xe00
	s_waitcnt lgkmcnt(6)
	v_mfma_f32_32x32x16_bf16 v[34:49], v[142:145], v[188:191], v[34:49]
	ds_read_b64_tr_b16 v[188:189], v156 offset:0x1600
	ds_read_b64_tr_b16 v[190:191], v156 offset:0x1e00
	s_waitcnt lgkmcnt(6)
	v_mfma_f32_32x32x16_bf16 v[34:49], v[172:175], v[192:195], v[34:49]
	ds_read_b64_tr_b16 v[192:193], v156 offset:0x2600
	ds_read_b64_tr_b16 v[194:195], v156 offset:0x2e00
	ds_read_b64_tr_b16 v[200:201], v156 offset:0x3600
	ds_read_b64_tr_b16 v[202:203], v156 offset:0x3e00
	s_waitcnt lgkmcnt(8)
	v_mfma_f32_32x32x16_bf16 v[34:49], v[176:179], v[196:199], v[34:49]
	s_waitcnt vmcnt(3) lgkmcnt(0)
	s_barrier
	v_mfma_f32_32x32x16_bf16 v[18:33], v[138:141], v[180:183], v[18:33]
	s_mov_b32 m0, s76
	s_nop 0
	global_load_lds_dwordx4 v253, s[10:11]
	s_mov_b32 m0, s77
	v_max_f32_e32 v132, v66, v66
	global_load_lds_dwordx4 v254, s[10:11]
	v_max_f32_e32 v131, v67, v67
	v_max_f32_e32 v131, v132, v131
	v_max3_f32 v131, v131, v68, v69
	v_max3_f32 v131, v131, v70, v71
	v_max3_f32 v131, v131, v72, v73
	v_max3_f32 v131, v131, v74, v75
	v_mfma_f32_32x32x16_bf16 v[18:33], v[142:145], v[188:191], v[18:33]
	v_max3_f32 v131, v131, v76, v77
	v_max3_f32 v131, v131, v78, v79
	v_max3_f32 v131, v131, v80, v81
	v_max3_f32 v131, v131, v82, v83
	v_max3_f32 v131, v131, v84, v85
	v_max3_f32 v131, v131, v86, v87
	v_max3_f32 v131, v131, v88, v89
	v_max3_f32 v131, v131, v90, v91
	v_mfma_f32_32x32x16_bf16 v[18:33], v[172:175], v[192:195], v[18:33]
	v_max3_f32 v131, v131, v92, v93
	v_max3_f32 v131, v131, v94, v95
	v_max3_f32 v131, v131, v96, v97
	v_mov_b32_e32 v132, v131
	s_nop 1
	v_permlane32_swap_b32_e32 v131, v132
	v_max_f32_e32 v132, v132, v132
	v_max_f32_e32 v131, v131, v131
	v_max_f32_e32 v131, v131, v132
	v_max_f32_e32 v133, v130, v130
	v_sub_f32_e32 v132, v131, v130
	v_max_f32_e32 v131, v133, v131
	v_mfma_f32_32x32x16_bf16 v[18:33], v[176:179], v[200:203], v[18:33]
	v_sub_f32_e32 v133, v130, v131
	v_mul_f32_e32 v133, 0x3dd53b94, v133
	v_exp_f32_e32 v133, v133
	v_cmp_ge_f32_e32 vcc, s65, v132
	s_cmp_eq_u64 vcc, exec
	s_cselect_b64 s[6:7], -1, 0
	v_cndmask_b32_e64 v166, v133, 1.0, s[6:7]
	v_cmp_gt_f32_e32 vcc, 1.0, v166
	s_cbranch_vccz .LBB0_1181
	s_and_saveexec_b64 s[10:11], s[4:5]
	ds_write_b32 v155, v166 offset:128
	s_or_b64 exec, exec, s[10:11]
	s_waitcnt lgkmcnt(0)
	v_add_u32_e32 v132, s69, v134
	ds_read_b128 v[138:141], v132 offset:224
	ds_read_b128 v[142:145], v132 offset:192
	ds_read_b128 v[172:175], v132 offset:160
	ds_read_b128 v[176:179], v132 offset:128
	s_waitcnt lgkmcnt(0)
	v_pk_mul_f32 v[14:15], v[14:15], v[138:139]
	v_pk_mul_f32 v[10:11], v[10:11], v[142:143]
	v_pk_mul_f32 v[6:7], v[6:7], v[172:173]
	v_pk_mul_f32 v[16:17], v[16:17], v[140:141]
	v_pk_mul_f32 v[12:13], v[12:13], v[144:145]
	v_pk_mul_f32 v[8:9], v[8:9], v[174:175]
	v_pk_mul_f32 v[4:5], v[4:5], v[178:179]
	v_pk_mul_f32 v[2:3], v[2:3], v[176:177]
	v_pk_mul_f32 v[62:63], v[62:63], v[138:139]
	v_pk_mul_f32 v[58:59], v[58:59], v[142:143]
	v_pk_mul_f32 v[54:55], v[54:55], v[172:173]
	v_pk_mul_f32 v[64:65], v[64:65], v[140:141]
	v_pk_mul_f32 v[60:61], v[60:61], v[144:145]
	v_pk_mul_f32 v[56:57], v[56:57], v[174:175]
	v_pk_mul_f32 v[52:53], v[52:53], v[178:179]
	v_pk_mul_f32 v[50:51], v[50:51], v[176:177]
	v_pk_mul_f32 v[46:47], v[46:47], v[138:139]
	v_pk_mul_f32 v[42:43], v[42:43], v[142:143]
	v_pk_mul_f32 v[38:39], v[38:39], v[172:173]
	v_pk_mul_f32 v[48:49], v[48:49], v[140:141]
	v_pk_mul_f32 v[44:45], v[44:45], v[144:145]
	v_pk_mul_f32 v[40:41], v[40:41], v[174:175]
	v_pk_mul_f32 v[36:37], v[36:37], v[178:179]
	v_pk_mul_f32 v[34:35], v[34:35], v[176:177]
	v_pk_mul_f32 v[30:31], v[30:31], v[138:139]
	v_pk_mul_f32 v[26:27], v[26:27], v[142:143]
	v_pk_mul_f32 v[22:23], v[22:23], v[172:173]
	v_pk_mul_f32 v[32:33], v[32:33], v[140:141]
	v_pk_mul_f32 v[28:29], v[28:29], v[144:145]
	v_pk_mul_f32 v[24:25], v[24:25], v[174:175]
	v_pk_mul_f32 v[20:21], v[20:21], v[178:179]
	v_pk_mul_f32 v[18:19], v[18:19], v[176:177]

.LBB0_1183:
	s_mul_i32 s7, s7, 0x12000
	s_sub_i32 s6, s8, s7
	s_addk_i32 s6, 0x6000
	v_add_u32_e32 v159, s6, v159
	ds_read_b128 v[66:69], v159 offset:32768
	ds_read_b128 v[186:189], v159 offset:32896
	ds_read_b128 v[82:85], v159 offset:45056
	ds_read_b128 v[190:193], v159 offset:33024
	v_add_u32_e32 v161, s6, v161
	s_waitcnt lgkmcnt(0)
	v_mfma_f32_32x32x16_bf16 v[66:81], v[66:69], v[126:129], 0
	v_add_u32_e32 v162, s6, v162
	v_add_u32_e32 v163, s6, v163
	v_exp_f32_e32 v146, v146
	v_exp_f32_e32 v147, v147
	v_exp_f32_e32 v144, v144
	v_exp_f32_e32 v145, v145
	v_exp_f32_e32 v142, v142
	v_mfma_f32_32x32x16_bf16 v[82:97], v[82:85], v[126:129], 0
	ds_read_b128 v[126:129], v161 offset:32768
	ds_read_b128 v[194:197], v161 offset:32896
	ds_read_b128 v[198:201], v161 offset:33024
	v_exp_f32_e32 v136, v136
	v_exp_f32_e32 v137, v137
	v_exp_f32_e32 v132, v132
	v_exp_f32_e32 v133, v133
	v_exp_f32_e32 v130, v130
	s_waitcnt lgkmcnt(0)
	v_mfma_f32_32x32x16_bf16 v[66:81], v[126:129], v[122:125], v[66:81]
	ds_read_b128 v[126:129], v161 offset:45056
	v_exp_f32_e32 v131, v131
	s_waitcnt lgkmcnt(0)
	v_mfma_f32_32x32x16_bf16 v[82:97], v[126:129], v[122:125], v[82:97]
	ds_read_b128 v[122:125], v162 offset:32768
	ds_read_b128 v[126:129], v162 offset:32896
	ds_read_b128 v[202:205], v162 offset:33024
	s_waitcnt lgkmcnt(0)
	v_mfma_f32_32x32x16_bf16 v[66:81], v[122:125], v[118:121], v[66:81]
	ds_read_b128 v[122:125], v162 offset:45056
	s_waitcnt lgkmcnt(0)
	v_mfma_f32_32x32x16_bf16 v[82:97], v[122:125], v[118:121], v[82:97]
	ds_read_b128 v[118:121], v163 offset:32768
	ds_read_b128 v[122:125], v163 offset:32896
	s_waitcnt lgkmcnt(0)
	v_mfma_f32_32x32x16_bf16 v[66:81], v[118:121], v[114:117], v[66:81]
	ds_read_b128 v[118:121], v163 offset:45056
	ds_read_b128 v[206:209], v163 offset:33024
	s_waitcnt lgkmcnt(0)
	v_mfma_f32_32x32x16_bf16 v[82:97], v[118:121], v[114:117], v[82:97]
	ds_read_b128 v[114:117], v159 offset:45184
	ds_read_b128 v[118:121], v159 offset:45312
	v_mfma_f32_32x32x16_bf16 v[66:81], v[186:189], v[110:113], v[66:81]
	s_waitcnt lgkmcnt(0)
	v_mfma_f32_32x32x16_bf16 v[82:97], v[114:117], v[110:113], v[82:97]
	ds_read_b128 v[110:113], v161 offset:45184
	v_mfma_f32_32x32x16_bf16 v[66:81], v[194:197], v[106:109], v[66:81]
	ds_read_b128 v[114:117], v161 offset:45312
	ds_read_b128 v[186:189], v158
	ds_read_b128 v[194:197], v158 offset:1024
	ds_read_b128 v[210:213], v162 offset:45184
	ds_read_b128 v[214:217], v162 offset:45312
	ds_read_b128 v[218:221], v163 offset:45184
	ds_read_b128 v[222:225], v163 offset:45312
	s_waitcnt lgkmcnt(0)
	v_mfma_f32_32x32x16_bf16 v[82:97], v[110:113], v[106:109], v[82:97]
	ds_read_b128 v[106:109], v158 offset:2048
	ds_read_b128 v[110:113], v158 offset:3072
	v_mfma_f32_32x32x16_bf16 v[66:81], v[126:129], v[102:105], v[66:81]
	v_exp_f32_e32 v126, v143
	v_exp_f32_e32 v127, v140
	v_exp_f32_e32 v128, v141
	v_exp_f32_e32 v129, v138
	v_exp_f32_e32 v138, v139
	v_mfma_f32_32x32x16_bf16 v[82:97], v[210:213], v[102:105], v[82:97]
	v_add_f32_e32 v102, 0, v178
	v_add_f32_e32 v102, v182, v102
	v_add_f32_e32 v102, v179, v102
	v_add_f32_e32 v102, v183, v102
	v_add_f32_e32 v102, v180, v102
	v_add_f32_e32 v102, v184, v102
	v_add_f32_e32 v102, v177, v102
	v_mfma_f32_32x32x16_bf16 v[66:81], v[122:125], v[98:101], v[66:81]
	v_add_f32_e32 v102, v181, v102
	v_add_f32_e32 v102, v171, v102
	v_add_f32_e32 v102, v175, v102
	v_mfma_f32_32x32x16_bf16 v[82:97], v[218:221], v[98:101], v[82:97]
	v_add_f32_e32 v98, v172, v102
	v_add_f32_e32 v98, v176, v98
	v_add_f32_e32 v98, v168, v98
	v_add_f32_e32 v98, v173, v98
	v_add_f32_e32 v98, v169, v98
	v_add_f32_e32 v98, v174, v98
	v_add_f32_e32 v98, v146, v98
	v_mfma_f32_32x32x16_bf16 v[66:81], v[190:193], v[186:189], v[66:81]
	v_add_f32_e32 v98, v147, v98
	v_add_f32_e32 v98, v144, v98
	v_add_f32_e32 v98, v145, v98
	v_add_f32_e32 v98, v142, v98
	v_add_f32_e32 v98, v126, v98
	v_add_f32_e32 v98, v127, v98
	v_add_f32_e32 v98, v128, v98
	v_mfma_f32_32x32x16_bf16 v[82:97], v[118:121], v[186:189], v[82:97]
	v_add_f32_e32 v98, v129, v98
	v_add_f32_e32 v98, v138, v98
	v_add_f32_e32 v98, v136, v98
	v_add_f32_e32 v98, v137, v98
	v_add_f32_e32 v98, v132, v98
	v_add_f32_e32 v98, v133, v98
	v_add_f32_e32 v98, v130, v98
	v_mfma_f32_32x32x16_bf16 v[66:81], v[198:201], v[194:197], v[66:81]
	v_add_f32_e32 v98, v131, v98
	v_mov_b32_e32 v99, v98
	v_cvt_pk_bf16_f32 v100, v178, v182
	v_cvt_pk_bf16_f32 v101, v179, v183
	v_cvt_pk_bf16_f32 v102, v180, v184
	v_cvt_pk_bf16_f32 v103, v177, v181
	s_nop 1
	v_permlane32_swap_b32_e32 v98, v99
	v_mfma_f32_32x32x16_bf16 v[82:97], v[114:117], v[194:197], v[82:97]
	v_permlane32_swap_b32_e32 v100, v102
	v_permlane32_swap_b32_e32 v101, v103
	v_cvt_pk_bf16_f32 v114, v171, v175
	v_cvt_pk_bf16_f32 v115, v172, v176
	v_cvt_pk_bf16_f32 v116, v168, v173
	s_waitcnt lgkmcnt(0)
	v_mfma_f32_32x32x16_bf16 v[66:81], v[202:205], v[106:109], v[66:81]
	v_cvt_pk_bf16_f32 v117, v169, v174
	v_cvt_pk_bf16_f32 v104, v146, v147
	v_cvt_pk_bf16_f32 v105, v144, v145
	v_permlane32_swap_b32_e32 v114, v116
	v_permlane32_swap_b32_e32 v115, v117
	v_mfma_f32_32x32x16_bf16 v[82:97], v[214:217], v[106:109], v[82:97]
	v_cvt_pk_bf16_f32 v106, v142, v126
	v_cvt_pk_bf16_f32 v107, v127, v128
	v_cvt_pk_bf16_f32 v118, v129, v138
	v_cvt_pk_bf16_f32 v119, v136, v137
	v_cvt_pk_bf16_f32 v120, v132, v133
	v_cvt_pk_bf16_f32 v121, v130, v131
	s_nop 0
	v_permlane32_swap_b32_e32 v104, v106
	v_mfma_f32_32x32x16_bf16 v[66:81], v[206:209], v[110:113], v[66:81]
	v_permlane32_swap_b32_e32 v105, v107
	v_permlane32_swap_b32_e32 v118, v120
	v_permlane32_swap_b32_e32 v119, v121
	v_mfma_f32_32x32x16_bf16 v[82:97], v[222:225], v[110:113], v[82:97]
	ds_read_b64_tr_b16 v[108:109], v160 offset:0
	ds_read_b64_tr_b16 v[110:111], v160 offset:0x800
	ds_read_b64_tr_b16 v[122:123], v160 offset:0x1000
	ds_read_b64_tr_b16 v[124:125], v160 offset:0x1800
	ds_read_b64_tr_b16 v[126:127], v160 offset:0x2000
	ds_read_b64_tr_b16 v[128:129], v160 offset:0x2800
	ds_read_b64_tr_b16 v[130:131], v160 offset:0x3000
	ds_read_b64_tr_b16 v[132:133], v160 offset:0x3800
	s_nop 0
	s_waitcnt lgkmcnt(6)
	v_mfma_f32_32x32x16_bf16 v[2:17], v[100:103], v[108:111], v[2:17]
	ds_read_b64_tr_b16 v[108:109], v160 offset:0x200
	ds_read_b64_tr_b16 v[110:111], v160 offset:0xa00
	s_waitcnt lgkmcnt(6)
	v_mfma_f32_32x32x16_bf16 v[2:17], v[114:117], v[122:125], v[2:17]
	ds_read_b64_tr_b16 v[122:123], v160 offset:0x1200
	ds_read_b64_tr_b16 v[124:125], v160 offset:0x1a00
	s_waitcnt lgkmcnt(6)
	v_mfma_f32_32x32x16_bf16 v[2:17], v[104:107], v[126:129], v[2:17]
	ds_read_b64_tr_b16 v[126:127], v160 offset:0x2200
	ds_read_b64_tr_b16 v[128:129], v160 offset:0x2a00
	ds_read_b64_tr_b16 v[136:137], v160 offset:0x3200
	ds_read_b64_tr_b16 v[138:139], v160 offset:0x3a00
	s_waitcnt lgkmcnt(8)
	v_mfma_f32_32x32x16_bf16 v[2:17], v[118:121], v[130:133], v[2:17]
	s_waitcnt lgkmcnt(6)
	v_mfma_f32_32x32x16_bf16 v[50:65], v[100:103], v[108:111], v[50:65]
	ds_read_b64_tr_b16 v[108:109], v160 offset:0x400
	ds_read_b64_tr_b16 v[110:111], v160 offset:0xc00
	s_waitcnt lgkmcnt(6)
	v_mfma_f32_32x32x16_bf16 v[50:65], v[114:117], v[122:125], v[50:65]
	ds_read_b64_tr_b16 v[122:123], v160 offset:0x1400
	ds_read_b64_tr_b16 v[124:125], v160 offset:0x1c00
	s_waitcnt lgkmcnt(6)
	v_mfma_f32_32x32x16_bf16 v[50:65], v[104:107], v[126:129], v[50:65]
	ds_read_b64_tr_b16 v[126:127], v160 offset:0x2400
	ds_read_b64_tr_b16 v[128:129], v160 offset:0x2c00
	ds_read_b64_tr_b16 v[130:131], v160 offset:0x3400
	ds_read_b64_tr_b16 v[132:133], v160 offset:0x3c00
	s_waitcnt lgkmcnt(8)
	v_mfma_f32_32x32x16_bf16 v[50:65], v[118:121], v[136:139], v[50:65]
	s_waitcnt lgkmcnt(6)
	v_mfma_f32_32x32x16_bf16 v[34:49], v[100:103], v[108:111], v[34:49]
	ds_read_b64_tr_b16 v[108:109], v160 offset:0x600
	ds_read_b64_tr_b16 v[110:111], v160 offset:0xe00
	s_waitcnt lgkmcnt(6)
	v_mfma_f32_32x32x16_bf16 v[34:49], v[114:117], v[122:125], v[34:49]
	ds_read_b64_tr_b16 v[122:123], v160 offset:0x1600
	ds_read_b64_tr_b16 v[124:125], v160 offset:0x1e00
	s_waitcnt lgkmcnt(6)
	v_mfma_f32_32x32x16_bf16 v[34:49], v[104:107], v[126:129], v[34:49]
	ds_read_b64_tr_b16 v[126:127], v160 offset:0x2600
	ds_read_b64_tr_b16 v[128:129], v160 offset:0x2e00
	ds_read_b64_tr_b16 v[136:137], v160 offset:0x3600
	ds_read_b64_tr_b16 v[138:139], v160 offset:0x3e00
	s_waitcnt lgkmcnt(8)
	v_mfma_f32_32x32x16_bf16 v[34:49], v[118:121], v[130:133], v[34:49]
	s_waitcnt lgkmcnt(6)
	v_mfma_f32_32x32x16_bf16 v[18:33], v[100:103], v[108:111], v[18:33]
	v_max_f32_e32 v112, v67, v67
	v_max_f32_e32 v113, v66, v66
	v_max_f32_e32 v112, v113, v112
	v_max3_f32 v112, v112, v68, v69
	v_max3_f32 v112, v112, v70, v71
	v_max3_f32 v100, v112, v72, v73
	v_max3_f32 v100, v100, v74, v75
	v_max3_f32 v100, v100, v76, v77
	s_waitcnt lgkmcnt(4)
	v_mfma_f32_32x32x16_bf16 v[18:33], v[114:117], v[122:125], v[18:33]
	v_max3_f32 v100, v100, v78, v79
	v_max3_f32 v100, v100, v80, v81
	v_max3_f32 v100, v100, v82, v83
	v_max3_f32 v100, v100, v84, v85
	v_max3_f32 v100, v100, v86, v87
	v_max3_f32 v100, v100, v88, v89
	v_max3_f32 v100, v100, v90, v91
	v_max3_f32 v100, v100, v92, v93
	s_waitcnt lgkmcnt(2)
	v_mfma_f32_32x32x16_bf16 v[18:33], v[104:107], v[126:129], v[18:33]
	v_max3_f32 v100, v100, v94, v95
	v_max3_f32 v100, v100, v96, v97
	v_mov_b32_e32 v101, v100
	s_nop 1
	v_permlane32_swap_b32_e32 v100, v101
	v_max_f32_e32 v101, v101, v101
	v_max_f32_e32 v100, v100, v100
	v_max_f32_e32 v100, v100, v101
	v_max_f32_e32 v101, v165, v165
	v_max_f32_e32 v101, v101, v100
	v_sub_f32_e32 v102, v100, v165
	s_waitcnt lgkmcnt(0)
	v_mfma_f32_32x32x16_bf16 v[18:33], v[118:121], v[136:139], v[18:33]
	v_sub_f32_e32 v100, v165, v101
	v_mul_f32_e32 v100, 0x3dd53b94, v100
	v_exp_f32_e32 v100, v100
	v_cmp_ge_f32_e32 vcc, s65, v102
	s_cmp_eq_u64 vcc, exec
	s_cselect_b64 s[6:7], -1, 0
	s_waitcnt vmcnt(0) lgkmcnt(0)
	s_barrier
	v_cndmask_b32_e64 v100, v100, 1.0, s[6:7]
	v_cmp_gt_f32_e32 vcc, 1.0, v100
	s_cbranch_vccz .LBB0_1187
	s_and_saveexec_b64 s[8:9], s[4:5]
	ds_write_b32 v155, v100 offset:128
	s_or_b64 exec, exec, s[8:9]
	s_waitcnt lgkmcnt(0)
	v_add_u32_e32 v114, s69, v134
	ds_read_b128 v[102:105], v114 offset:224
	ds_read_b128 v[106:109], v114 offset:192
	ds_read_b128 v[110:113], v114 offset:160
	ds_read_b128 v[114:117], v114 offset:128
	s_waitcnt lgkmcnt(0)
	v_pk_mul_f32 v[14:15], v[14:15], v[102:103]
	v_pk_mul_f32 v[10:11], v[10:11], v[106:107]
	v_pk_mul_f32 v[6:7], v[6:7], v[110:111]
	v_pk_mul_f32 v[16:17], v[16:17], v[104:105]
	v_pk_mul_f32 v[12:13], v[12:13], v[108:109]
	v_pk_mul_f32 v[8:9], v[8:9], v[112:113]
	v_pk_mul_f32 v[4:5], v[4:5], v[116:117]
	v_pk_mul_f32 v[2:3], v[2:3], v[114:115]
	v_pk_mul_f32 v[62:63], v[62:63], v[102:103]
	v_pk_mul_f32 v[58:59], v[58:59], v[106:107]
	v_pk_mul_f32 v[54:55], v[54:55], v[110:111]
	v_pk_mul_f32 v[64:65], v[64:65], v[104:105]
	v_pk_mul_f32 v[60:61], v[60:61], v[108:109]
	v_pk_mul_f32 v[56:57], v[56:57], v[112:113]
	v_pk_mul_f32 v[52:53], v[52:53], v[116:117]
	v_pk_mul_f32 v[50:51], v[50:51], v[114:115]
	v_pk_mul_f32 v[46:47], v[46:47], v[102:103]
	v_pk_mul_f32 v[42:43], v[42:43], v[106:107]
	v_pk_mul_f32 v[38:39], v[38:39], v[110:111]
	v_pk_mul_f32 v[48:49], v[48:49], v[104:105]
	v_pk_mul_f32 v[44:45], v[44:45], v[108:109]
	v_pk_mul_f32 v[40:41], v[40:41], v[112:113]
	v_pk_mul_f32 v[36:37], v[36:37], v[116:117]
	v_pk_mul_f32 v[34:35], v[34:35], v[114:115]
	v_pk_mul_f32 v[30:31], v[30:31], v[102:103]
	v_pk_mul_f32 v[26:27], v[26:27], v[106:107]
	v_pk_mul_f32 v[22:23], v[22:23], v[110:111]
	v_pk_mul_f32 v[32:33], v[32:33], v[104:105]
	v_pk_mul_f32 v[28:29], v[28:29], v[108:109]
	v_pk_mul_f32 v[24:25], v[24:25], v[112:113]
	v_pk_mul_f32 v[20:21], v[20:21], v[116:117]
	v_pk_mul_f32 v[18:19], v[18:19], v[114:115]
.LBB0_1187:
	v_cndmask_b32_e64 v101, v101, v165, s[6:7]
	v_mul_f32_e32 v101, 0xbdd53b94, v101
	v_fmamk_f32 v66, v66, 0x3dd53b94, v101
	v_fmamk_f32 v67, v67, 0x3dd53b94, v101
	v_fmamk_f32 v68, v68, 0x3dd53b94, v101
	v_fmamk_f32 v69, v69, 0x3dd53b94, v101
	v_fmamk_f32 v70, v70, 0x3dd53b94, v101
	v_fmamk_f32 v71, v71, 0x3dd53b94, v101
	v_fmamk_f32 v72, v72, 0x3dd53b94, v101
	v_fmamk_f32 v73, v73, 0x3dd53b94, v101
	v_fmamk_f32 v74, v74, 0x3dd53b94, v101
	v_fmamk_f32 v75, v75, 0x3dd53b94, v101
	v_fmamk_f32 v76, v76, 0x3dd53b94, v101
	v_fmamk_f32 v77, v77, 0x3dd53b94, v101
	v_fmamk_f32 v78, v78, 0x3dd53b94, v101
	v_fmamk_f32 v79, v79, 0x3dd53b94, v101
	v_fmamk_f32 v80, v80, 0x3dd53b94, v101
	v_fmamk_f32 v81, v81, 0x3dd53b94, v101
	v_fmamk_f32 v82, v82, 0x3dd53b94, v101
	v_fmamk_f32 v83, v83, 0x3dd53b94, v101
	v_fmamk_f32 v84, v84, 0x3dd53b94, v101
	v_fmamk_f32 v85, v85, 0x3dd53b94, v101
	v_fmamk_f32 v86, v86, 0x3dd53b94, v101
	v_fmamk_f32 v87, v87, 0x3dd53b94, v101
	v_fmamk_f32 v88, v88, 0x3dd53b94, v101
	v_fmamk_f32 v89, v89, 0x3dd53b94, v101
	v_fmamk_f32 v90, v90, 0x3dd53b94, v101
	v_fmamk_f32 v91, v91, 0x3dd53b94, v101
	v_fmamk_f32 v92, v92, 0x3dd53b94, v101
	v_fmamk_f32 v93, v93, 0x3dd53b94, v101
	v_fmamk_f32 v94, v94, 0x3dd53b94, v101
	v_fmamk_f32 v95, v95, 0x3dd53b94, v101
	v_fmamk_f32 v96, v96, 0x3dd53b94, v101
	v_fmac_f32_e32 v101, 0x3dd53b94, v97
	v_exp_f32_e32 v97, v66
	v_exp_f32_e32 v102, v67
	v_exp_f32_e32 v103, v68
	v_exp_f32_e32 v69, v69
	v_exp_f32_e32 v70, v70
	v_add_f32_e32 v66, 0, v97
	v_exp_f32_e32 v71, v71
	v_add_f32_e32 v66, v102, v66
	v_exp_f32_e32 v72, v72
	v_add_f32_e32 v66, v103, v66
	v_exp_f32_e32 v73, v73
	v_add_f32_e32 v66, v69, v66
	v_exp_f32_e32 v74, v74
	v_add_f32_e32 v66, v70, v66
	v_exp_f32_e32 v75, v75
	v_add_f32_e32 v66, v71, v66
	v_exp_f32_e32 v76, v76
	v_add_f32_e32 v66, v72, v66
	v_exp_f32_e32 v77, v77
	v_add_f32_e32 v66, v73, v66
	v_exp_f32_e32 v78, v78
	v_add_f32_e32 v66, v74, v66
	v_exp_f32_e32 v79, v79
	v_add_f32_e32 v66, v75, v66
	v_exp_f32_e32 v80, v80
	v_add_f32_e32 v66, v76, v66
	v_exp_f32_e32 v81, v81
	v_add_f32_e32 v66, v77, v66
	v_exp_f32_e32 v82, v82
	v_add_f32_e32 v66, v78, v66
	v_exp_f32_e32 v83, v83
	v_add_f32_e32 v66, v79, v66
	v_exp_f32_e32 v84, v84
	v_add_f32_e32 v66, v80, v66
	v_exp_f32_e32 v85, v85
	v_add_f32_e32 v66, v81, v66
	v_exp_f32_e32 v86, v86
	v_add_f32_e32 v66, v82, v66
	v_exp_f32_e32 v87, v87
	v_add_f32_e32 v66, v83, v66
	v_exp_f32_e32 v88, v88
	v_add_f32_e32 v66, v84, v66
	v_exp_f32_e32 v89, v89
	v_add_f32_e32 v66, v85, v66
	v_exp_f32_e32 v90, v90
	v_add_f32_e32 v66, v86, v66
	v_exp_f32_e32 v91, v91
	v_add_f32_e32 v66, v87, v66
	v_exp_f32_e32 v92, v92
	v_add_f32_e32 v66, v88, v66
	v_exp_f32_e32 v93, v93
	v_add_f32_e32 v66, v89, v66
	v_exp_f32_e32 v94, v94
	v_add_f32_e32 v66, v90, v66
	v_exp_f32_e32 v95, v95
	v_add_f32_e32 v66, v91, v66
	v_exp_f32_e32 v96, v96
	v_add_f32_e32 v66, v92, v66
	v_exp_f32_e32 v101, v101
	v_add_f32_e32 v66, v93, v66
	v_add_f32_e32 v66, v94, v66
	v_add_f32_e32 v66, v95, v66
	v_add_f32_e32 v66, v96, v66
	v_add_f32_e32 v66, v101, v66
	v_mov_b32_e32 v67, v66
	s_nop 1
	v_permlane32_swap_b32_e32 v66, v67
	v_cvt_pk_bf16_f32 v68, v97, v102
	v_cvt_pk_bf16_f32 v69, v103, v69
	v_cvt_pk_bf16_f32 v70, v70, v71
	v_cvt_pk_bf16_f32 v71, v72, v73
	v_cvt_pk_bf16_f32 v72, v74, v75
	v_cvt_pk_bf16_f32 v73, v76, v77
	v_cvt_pk_bf16_f32 v74, v78, v79
	v_cvt_pk_bf16_f32 v75, v80, v81
	v_cvt_pk_bf16_f32 v76, v82, v83
	v_cvt_pk_bf16_f32 v77, v84, v85
	v_cvt_pk_bf16_f32 v78, v86, v87
	v_cvt_pk_bf16_f32 v79, v88, v89
	v_cvt_pk_bf16_f32 v80, v90, v91
	v_cvt_pk_bf16_f32 v81, v92, v93
	v_cvt_pk_bf16_f32 v82, v94, v95
	v_cvt_pk_bf16_f32 v83, v96, v101
	s_nop 0
	v_permlane32_swap_b32_e32 v68, v70
	v_permlane32_swap_b32_e32 v69, v71
	v_permlane32_swap_b32_e32 v72, v74
	v_permlane32_swap_b32_e32 v73, v75
	v_permlane32_swap_b32_e32 v76, v78
	v_permlane32_swap_b32_e32 v77, v79
	v_permlane32_swap_b32_e32 v80, v82
	v_permlane32_swap_b32_e32 v81, v83
	ds_read_b64_tr_b16 v[84:85], v156 offset:0
	ds_read_b64_tr_b16 v[86:87], v156 offset:0x800
	ds_read_b64_tr_b16 v[88:89], v156 offset:0x1000
	ds_read_b64_tr_b16 v[90:91], v156 offset:0x1800
	ds_read_b64_tr_b16 v[92:93], v156 offset:0x2000
	ds_read_b64_tr_b16 v[94:95], v156 offset:0x2800
	ds_read_b64_tr_b16 v[102:103], v156 offset:0x3000
	ds_read_b64_tr_b16 v[104:105], v156 offset:0x3800
	s_nop 0
	s_waitcnt lgkmcnt(6)
	v_mfma_f32_32x32x16_bf16 v[2:17], v[68:71], v[84:87], v[2:17]
	ds_read_b64_tr_b16 v[84:85], v156 offset:0x200
	ds_read_b64_tr_b16 v[86:87], v156 offset:0xa00
	s_waitcnt lgkmcnt(6)
	v_mfma_f32_32x32x16_bf16 v[2:17], v[72:75], v[88:91], v[2:17]
	ds_read_b64_tr_b16 v[88:89], v156 offset:0x1200
	ds_read_b64_tr_b16 v[90:91], v156 offset:0x1a00
	s_waitcnt lgkmcnt(6)
	v_mfma_f32_32x32x16_bf16 v[2:17], v[76:79], v[92:95], v[2:17]
	ds_read_b64_tr_b16 v[92:93], v156 offset:0x2200
	ds_read_b64_tr_b16 v[94:95], v156 offset:0x2a00
	ds_read_b64_tr_b16 v[106:107], v156 offset:0x3200
	ds_read_b64_tr_b16 v[108:109], v156 offset:0x3a00
	s_waitcnt lgkmcnt(8)
	v_mfma_f32_32x32x16_bf16 v[2:17], v[80:83], v[102:105], v[2:17]
	s_waitcnt lgkmcnt(6)
	v_mfma_f32_32x32x16_bf16 v[50:65], v[68:71], v[84:87], v[50:65]
	ds_read_b64_tr_b16 v[84:85], v156 offset:0x400
	ds_read_b64_tr_b16 v[86:87], v156 offset:0xc00
	s_waitcnt lgkmcnt(6)
	v_mfma_f32_32x32x16_bf16 v[50:65], v[72:75], v[88:91], v[50:65]
	ds_read_b64_tr_b16 v[88:89], v156 offset:0x1400
	ds_read_b64_tr_b16 v[90:91], v156 offset:0x1c00
	s_waitcnt lgkmcnt(6)
	v_mfma_f32_32x32x16_bf16 v[50:65], v[76:79], v[92:95], v[50:65]
	ds_read_b64_tr_b16 v[92:93], v156 offset:0x2400
	ds_read_b64_tr_b16 v[94:95], v156 offset:0x2c00
	ds_read_b64_tr_b16 v[102:103], v156 offset:0x3400
	ds_read_b64_tr_b16 v[104:105], v156 offset:0x3c00
	s_waitcnt lgkmcnt(8)
	v_mfma_f32_32x32x16_bf16 v[50:65], v[80:83], v[106:109], v[50:65]
	s_waitcnt lgkmcnt(6)
	v_mfma_f32_32x32x16_bf16 v[34:49], v[68:71], v[84:87], v[34:49]
	ds_read_b64_tr_b16 v[84:85], v156 offset:0x600
	ds_read_b64_tr_b16 v[86:87], v156 offset:0xe00
	s_waitcnt lgkmcnt(6)
	v_mfma_f32_32x32x16_bf16 v[34:49], v[72:75], v[88:91], v[34:49]
	ds_read_b64_tr_b16 v[88:89], v156 offset:0x1600
	ds_read_b64_tr_b16 v[90:91], v156 offset:0x1e00
	s_waitcnt lgkmcnt(6)
	v_mfma_f32_32x32x16_bf16 v[34:49], v[76:79], v[92:95], v[34:49]
	ds_read_b64_tr_b16 v[92:93], v156 offset:0x2600
	ds_read_b64_tr_b16 v[94:95], v156 offset:0x2e00
	ds_read_b64_tr_b16 v[106:107], v156 offset:0x3600
	ds_read_b64_tr_b16 v[108:109], v156 offset:0x3e00
	s_waitcnt lgkmcnt(8)
	v_mfma_f32_32x32x16_bf16 v[34:49], v[80:83], v[102:105], v[34:49]
	s_waitcnt lgkmcnt(6)
	v_mfma_f32_32x32x16_bf16 v[18:33], v[68:71], v[84:87], v[18:33]
	s_waitcnt lgkmcnt(4)
	v_mfma_f32_32x32x16_bf16 v[18:33], v[72:75], v[88:91], v[18:33]
	s_waitcnt lgkmcnt(2)
	v_mfma_f32_32x32x16_bf16 v[18:33], v[76:79], v[92:95], v[18:33]
	s_waitcnt lgkmcnt(0)
	v_mfma_f32_32x32x16_bf16 v[18:33], v[80:83], v[106:109], v[18:33]
	s_and_saveexec_b64 s[6:7], s[4:5]
	s_cbranch_execz .LBB0_1164
	v_add_f32_e32 v68, v98, v99
	v_fmac_f32_e32 v68, v157, v166
	v_add_f32_e32 v66, v66, v67
	v_fmac_f32_e32 v66, v68, v100
	ds_write_b32 v155, v66
	s_branch .LBB0_1164
